# accumulator zeroing before each GEMM K loop uses 64 v_mov_b64 instead of 128 v_mov_b32
# speedup vs baseline: 1.0068x; 1.0068x over previous
.LBB0_227:
	s_ashr_i32 s47, s46, 31
	s_lshl_b64 s[50:51], s[46:47], 19
	s_add_u32 s50, s21, s50
	s_addc_u32 s51, s22, s51
	s_ashr_i32 s43, s42, 31
	s_lshl_b64 s[52:53], s[42:43], 19
	s_add_u32 s52, s15, s52
	s_addc_u32 s53, s20, s53
	s_andn2_b64 vcc, exec, s[30:31]
	s_cbranch_vccnz .LBB0_269
	s_and_b64 s[62:63], s[48:49], exec
	s_cselect_b32 s39, s51, s59
	s_cselect_b32 s43, s50, s58
	s_cselect_b32 s47, s53, s61
	s_cselect_b32 s55, s52, s60
	s_add_u32 s71, s60, 0x100
	s_addc_u32 s72, s61, 0
	s_add_u32 s58, s58, 0x40080
	v_mov_b64_e32 v[34:35], 0
	v_mov_b32_e32 v1, 0x3ecc95a3
	s_addc_u32 s59, s59, 0
	s_mov_b32 s60, 0
	v_mov_b64_e32 v[36:37], 0
	v_mov_b64_e32 v[38:39], 0
	v_mov_b64_e32 v[40:41], 0
	v_mov_b64_e32 v[50:51], 0
	v_mov_b64_e32 v[52:53], 0
	v_mov_b64_e32 v[54:55], 0
	v_mov_b64_e32 v[56:57], 0
	v_mov_b64_e32 v[10:11], 0
	v_mov_b64_e32 v[12:13], 0
	v_mov_b64_e32 v[14:15], 0
	v_mov_b64_e32 v[16:17], 0
	v_mov_b64_e32 v[26:27], 0
	v_mov_b64_e32 v[28:29], 0
	v_mov_b64_e32 v[30:31], 0
	v_mov_b64_e32 v[32:33], 0
	v_mov_b64_e32 v[42:43], 0
	v_mov_b64_e32 v[44:45], 0
	v_mov_b64_e32 v[46:47], 0
	v_mov_b64_e32 v[48:49], 0
	v_mov_b64_e32 v[58:59], 0
	v_mov_b64_e32 v[60:61], 0
	v_mov_b64_e32 v[62:63], 0
	v_mov_b64_e32 v[64:65], 0
	v_mov_b64_e32 v[66:67], 0
	v_mov_b64_e32 v[68:69], 0
	v_mov_b64_e32 v[70:71], 0
	v_mov_b64_e32 v[72:73], 0
	v_mov_b64_e32 v[82:83], 0
	v_mov_b64_e32 v[84:85], 0
	v_mov_b64_e32 v[86:87], 0
	v_mov_b64_e32 v[88:89], 0
	v_mov_b64_e32 v[98:99], 0
	v_mov_b64_e32 v[100:101], 0
	v_mov_b64_e32 v[102:103], 0
	v_mov_b64_e32 v[104:105], 0
	v_mov_b64_e32 v[114:115], 0
	v_mov_b64_e32 v[116:117], 0
	v_mov_b64_e32 v[118:119], 0
	v_mov_b64_e32 v[120:121], 0
	v_mov_b64_e32 v[74:75], 0
	v_mov_b64_e32 v[76:77], 0
	v_mov_b64_e32 v[78:79], 0
	v_mov_b64_e32 v[80:81], 0
	v_mov_b64_e32 v[90:91], 0
	v_mov_b64_e32 v[92:93], 0
	v_mov_b64_e32 v[94:95], 0
	v_mov_b64_e32 v[96:97], 0
	v_mov_b64_e32 v[106:107], 0
	v_mov_b64_e32 v[108:109], 0
	v_mov_b64_e32 v[110:111], 0
	v_mov_b64_e32 v[112:113], 0
	v_mov_b64_e32 v[122:123], 0
	v_mov_b64_e32 v[124:125], 0
	v_mov_b64_e32 v[126:127], 0
	v_mov_b64_e32 v[128:129], 0
	v_mov_b64_e32 v[22:23], 0
	v_mov_b64_e32 v[24:25], 0
	v_mov_b64_e32 v[18:19], 0
	v_mov_b64_e32 v[20:21], 0
	v_mov_b64_e32 v[6:7], 0
	v_mov_b64_e32 v[8:9], 0
	v_mov_b64_e32 v[2:3], 0
	v_mov_b64_e32 v[4:5], 0

.LBB0_269:
	v_mov_b64_e32 v[4:5], 0
	v_mov_b64_e32 v[2:3], 0
	v_mov_b64_e32 v[8:9], 0
	v_mov_b64_e32 v[6:7], 0
	v_mov_b64_e32 v[20:21], 0
	v_mov_b64_e32 v[18:19], 0
	v_mov_b64_e32 v[24:25], 0
	v_mov_b64_e32 v[22:23], 0
	v_mov_b64_e32 v[128:129], 0
	v_mov_b64_e32 v[126:127], 0
	v_mov_b64_e32 v[124:125], 0
	v_mov_b64_e32 v[122:123], 0
	v_mov_b64_e32 v[112:113], 0
	v_mov_b64_e32 v[110:111], 0
	v_mov_b64_e32 v[108:109], 0
	v_mov_b64_e32 v[106:107], 0
	v_mov_b64_e32 v[96:97], 0
	v_mov_b64_e32 v[94:95], 0
	v_mov_b64_e32 v[92:93], 0
	v_mov_b64_e32 v[90:91], 0
	v_mov_b64_e32 v[80:81], 0
	v_mov_b64_e32 v[78:79], 0
	v_mov_b64_e32 v[76:77], 0
	v_mov_b64_e32 v[74:75], 0
	v_mov_b64_e32 v[120:121], 0
	v_mov_b64_e32 v[118:119], 0
	v_mov_b64_e32 v[116:117], 0
	v_mov_b64_e32 v[114:115], 0
	v_mov_b64_e32 v[104:105], 0
	v_mov_b64_e32 v[102:103], 0
	v_mov_b64_e32 v[100:101], 0
	v_mov_b64_e32 v[98:99], 0
	v_mov_b64_e32 v[88:89], 0
	v_mov_b64_e32 v[86:87], 0
	v_mov_b64_e32 v[84:85], 0
	v_mov_b64_e32 v[82:83], 0
	v_mov_b64_e32 v[72:73], 0
	v_mov_b64_e32 v[70:71], 0
	v_mov_b64_e32 v[68:69], 0
	v_mov_b64_e32 v[66:67], 0
	v_mov_b64_e32 v[64:65], 0
	v_mov_b64_e32 v[62:63], 0
	v_mov_b64_e32 v[60:61], 0
	v_mov_b64_e32 v[58:59], 0
	v_mov_b64_e32 v[48:49], 0
	v_mov_b64_e32 v[46:47], 0
	v_mov_b64_e32 v[44:45], 0
	v_mov_b64_e32 v[42:43], 0
	v_mov_b64_e32 v[32:33], 0
	v_mov_b64_e32 v[30:31], 0
	v_mov_b64_e32 v[28:29], 0
	v_mov_b64_e32 v[26:27], 0
	v_mov_b64_e32 v[16:17], 0
	v_mov_b64_e32 v[14:15], 0
	v_mov_b64_e32 v[12:13], 0
	v_mov_b64_e32 v[10:11], 0
	v_mov_b64_e32 v[56:57], 0
	v_mov_b64_e32 v[54:55], 0
	v_mov_b64_e32 v[52:53], 0
	v_mov_b64_e32 v[50:51], 0
	v_mov_b64_e32 v[40:41], 0
	v_mov_b64_e32 v[38:39], 0
	v_mov_b64_e32 v[36:37], 0
	v_mov_b64_e32 v[34:35], 0
	s_and_b64 vcc, exec, s[34:35]
	s_cbranch_vccnz .LBB0_231
	s_branch .LBB0_232

.LBB0_296:
	s_ashr_i32 s43, s42, 31
	s_lshl_b64 s[48:49], s[42:43], 18
	s_add_u32 s48, s21, s48
	s_addc_u32 s49, s22, s49
	s_ashr_i32 s41, s40, 31
	s_lshl_b64 s[50:51], s[40:41], 18
	s_add_u32 s50, s15, s50
	s_addc_u32 s51, s20, s51
	s_andn2_b64 vcc, exec, s[30:31]
	s_cbranch_vccnz .LBB0_336
	s_and_b64 s[60:61], s[46:47], exec
	s_cselect_b32 s39, s49, s55
	s_cselect_b32 s41, s48, s54
	s_cselect_b32 s43, s51, s59
	s_cselect_b32 s53, s50, s58
	s_add_u32 s69, s58, 0x100
	s_addc_u32 s70, s59, 0
	s_add_u32 s54, s54, 0x20080
	v_mov_b64_e32 v[66:67], 0
	v_mov_b32_e32 v1, 0x3ecc95a3
	s_addc_u32 s55, s55, 0
	s_mov_b32 s58, 0
	v_mov_b64_e32 v[68:69], 0
	v_mov_b64_e32 v[70:71], 0
	v_mov_b64_e32 v[72:73], 0
	v_mov_b64_e32 v[82:83], 0
	v_mov_b64_e32 v[84:85], 0
	v_mov_b64_e32 v[86:87], 0
	v_mov_b64_e32 v[88:89], 0
	v_mov_b64_e32 v[42:43], 0
	v_mov_b64_e32 v[44:45], 0
	v_mov_b64_e32 v[46:47], 0
	v_mov_b64_e32 v[48:49], 0
	v_mov_b64_e32 v[58:59], 0
	v_mov_b64_e32 v[60:61], 0
	v_mov_b64_e32 v[62:63], 0
	v_mov_b64_e32 v[64:65], 0
	v_mov_b64_e32 v[74:75], 0
	v_mov_b64_e32 v[76:77], 0
	v_mov_b64_e32 v[78:79], 0
	v_mov_b64_e32 v[80:81], 0
	v_mov_b64_e32 v[90:91], 0
	v_mov_b64_e32 v[92:93], 0
	v_mov_b64_e32 v[94:95], 0
	v_mov_b64_e32 v[96:97], 0
	v_mov_b64_e32 v[98:99], 0
	v_mov_b64_e32 v[100:101], 0
	v_mov_b64_e32 v[102:103], 0
	v_mov_b64_e32 v[104:105], 0
	v_mov_b64_e32 v[114:115], 0
	v_mov_b64_e32 v[116:117], 0
	v_mov_b64_e32 v[118:119], 0
	v_mov_b64_e32 v[120:121], 0
	v_mov_b64_e32 v[130:131], 0
	v_mov_b64_e32 v[132:133], 0
	v_mov_b64_e32 v[134:135], 0
	v_mov_b64_e32 v[136:137], 0
	v_mov_b64_e32 v[146:147], 0
	v_mov_b64_e32 v[148:149], 0
	v_mov_b64_e32 v[150:151], 0
	v_mov_b64_e32 v[152:153], 0
	v_mov_b64_e32 v[106:107], 0
	v_mov_b64_e32 v[108:109], 0
	v_mov_b64_e32 v[110:111], 0
	v_mov_b64_e32 v[112:113], 0
	v_mov_b64_e32 v[122:123], 0
	v_mov_b64_e32 v[124:125], 0
	v_mov_b64_e32 v[126:127], 0
	v_mov_b64_e32 v[128:129], 0
	v_mov_b64_e32 v[138:139], 0
	v_mov_b64_e32 v[140:141], 0
	v_mov_b64_e32 v[142:143], 0
	v_mov_b64_e32 v[144:145], 0
	v_mov_b64_e32 v[154:155], 0
	v_mov_b64_e32 v[156:157], 0
	v_mov_b64_e32 v[158:159], 0
	v_mov_b64_e32 v[160:161], 0
	v_mov_b64_e32 v[54:55], 0
	v_mov_b64_e32 v[56:57], 0
	v_mov_b64_e32 v[50:51], 0
	v_mov_b64_e32 v[52:53], 0
	v_mov_b64_e32 v[38:39], 0
	v_mov_b64_e32 v[40:41], 0
	v_mov_b64_e32 v[34:35], 0
	v_mov_b64_e32 v[36:37], 0

.LBB0_336:
	v_mov_b64_e32 v[36:37], 0
	v_mov_b64_e32 v[34:35], 0
	v_mov_b64_e32 v[40:41], 0
	v_mov_b64_e32 v[38:39], 0
	v_mov_b64_e32 v[52:53], 0
	v_mov_b64_e32 v[50:51], 0
	v_mov_b64_e32 v[56:57], 0
	v_mov_b64_e32 v[54:55], 0
	v_mov_b64_e32 v[160:161], 0
	v_mov_b64_e32 v[158:159], 0
	v_mov_b64_e32 v[156:157], 0
	v_mov_b64_e32 v[154:155], 0
	v_mov_b64_e32 v[144:145], 0
	v_mov_b64_e32 v[142:143], 0
	v_mov_b64_e32 v[140:141], 0
	v_mov_b64_e32 v[138:139], 0
	v_mov_b64_e32 v[128:129], 0
	v_mov_b64_e32 v[126:127], 0
	v_mov_b64_e32 v[124:125], 0
	v_mov_b64_e32 v[122:123], 0
	v_mov_b64_e32 v[112:113], 0
	v_mov_b64_e32 v[110:111], 0
	v_mov_b64_e32 v[108:109], 0
	v_mov_b64_e32 v[106:107], 0
	v_mov_b64_e32 v[152:153], 0
	v_mov_b64_e32 v[150:151], 0
	v_mov_b64_e32 v[148:149], 0
	v_mov_b64_e32 v[146:147], 0
	v_mov_b64_e32 v[136:137], 0
	v_mov_b64_e32 v[134:135], 0
	v_mov_b64_e32 v[132:133], 0
	v_mov_b64_e32 v[130:131], 0
	v_mov_b64_e32 v[120:121], 0
	v_mov_b64_e32 v[118:119], 0
	v_mov_b64_e32 v[116:117], 0
	v_mov_b64_e32 v[114:115], 0
	v_mov_b64_e32 v[104:105], 0
	v_mov_b64_e32 v[102:103], 0
	v_mov_b64_e32 v[100:101], 0
	v_mov_b64_e32 v[98:99], 0
	v_mov_b64_e32 v[96:97], 0
	v_mov_b64_e32 v[94:95], 0
	v_mov_b64_e32 v[92:93], 0
	v_mov_b64_e32 v[90:91], 0
	v_mov_b64_e32 v[80:81], 0
	v_mov_b64_e32 v[78:79], 0
	v_mov_b64_e32 v[76:77], 0
	v_mov_b64_e32 v[74:75], 0
	v_mov_b64_e32 v[64:65], 0
	v_mov_b64_e32 v[62:63], 0
	v_mov_b64_e32 v[60:61], 0
	v_mov_b64_e32 v[58:59], 0
	v_mov_b64_e32 v[48:49], 0
	v_mov_b64_e32 v[46:47], 0
	v_mov_b64_e32 v[44:45], 0
	v_mov_b64_e32 v[42:43], 0
	v_mov_b64_e32 v[88:89], 0
	v_mov_b64_e32 v[86:87], 0
	v_mov_b64_e32 v[84:85], 0
	v_mov_b64_e32 v[82:83], 0
	v_mov_b64_e32 v[72:73], 0
	v_mov_b64_e32 v[70:71], 0
	v_mov_b64_e32 v[68:69], 0
	v_mov_b64_e32 v[66:67], 0
	s_and_b64 vcc, exec, s[34:35]
	s_cbranch_vccnz .LBB0_300
	s_branch .LBB0_301

.LBB0_467:
	s_lshl_b64 s[60:61], s[50:51], 16
	s_add_u32 s60, s11, s60
	s_addc_u32 s61, s12, s61
	s_andn2_b64 vcc, exec, s[40:41]
	s_cbranch_vccnz .LBB0_470
	s_and_b64 s[70:71], exec, s[54:55]
	s_cselect_b32 s51, s61, s69
	s_cselect_b32 s53, s60, s68
	s_add_u32 s66, s68, 0x100
	s_addc_u32 s72, s69, 0
	s_add_u32 s64, s64, 0x40080
	v_mov_b64_e32 v[18:19], 0
	s_addc_u32 s65, s65, 0
	s_mov_b32 s68, 0
	v_mov_b64_e32 v[20:21], 0
	v_mov_b64_e32 v[82:83], 0
	v_mov_b64_e32 v[84:85], 0
	v_mov_b64_e32 v[26:27], 0
	v_mov_b64_e32 v[28:29], 0
	v_mov_b64_e32 v[90:91], 0
	v_mov_b64_e32 v[92:93], 0
	v_mov_b64_e32 v[6:7], 0
	v_mov_b64_e32 v[8:9], 0
	v_mov_b64_e32 v[70:71], 0
	v_mov_b64_e32 v[72:73], 0
	v_mov_b64_e32 v[14:15], 0
	v_mov_b64_e32 v[16:17], 0
	v_mov_b64_e32 v[78:79], 0
	v_mov_b64_e32 v[80:81], 0
	v_mov_b64_e32 v[22:23], 0
	v_mov_b64_e32 v[24:25], 0
	v_mov_b64_e32 v[86:87], 0
	v_mov_b64_e32 v[88:89], 0
	v_mov_b64_e32 v[30:31], 0
	v_mov_b64_e32 v[32:33], 0
	v_mov_b64_e32 v[94:95], 0
	v_mov_b64_e32 v[96:97], 0
	v_mov_b64_e32 v[34:35], 0
	v_mov_b64_e32 v[36:37], 0
	v_mov_b64_e32 v[98:99], 0
	v_mov_b64_e32 v[100:101], 0
	v_mov_b64_e32 v[42:43], 0
	v_mov_b64_e32 v[44:45], 0
	v_mov_b64_e32 v[118:119], 0
	v_mov_b64_e32 v[120:121], 0
	v_mov_b64_e32 v[50:51], 0
	v_mov_b64_e32 v[52:53], 0
	v_mov_b64_e32 v[126:127], 0
	v_mov_b64_e32 v[128:129], 0
	v_mov_b64_e32 v[58:59], 0
	v_mov_b64_e32 v[60:61], 0
	v_mov_b64_e32 v[134:135], 0
	v_mov_b64_e32 v[136:137], 0
	v_mov_b64_e32 v[38:39], 0
	v_mov_b64_e32 v[40:41], 0
	v_mov_b64_e32 v[102:103], 0
	v_mov_b64_e32 v[104:105], 0
	v_mov_b64_e32 v[46:47], 0
	v_mov_b64_e32 v[48:49], 0
	v_mov_b64_e32 v[122:123], 0
	v_mov_b64_e32 v[124:125], 0
	v_mov_b64_e32 v[54:55], 0
	v_mov_b64_e32 v[56:57], 0
	v_mov_b64_e32 v[130:131], 0
	v_mov_b64_e32 v[132:133], 0
	v_mov_b64_e32 v[62:63], 0
	v_mov_b64_e32 v[64:65], 0
	v_mov_b64_e32 v[138:139], 0
	v_mov_b64_e32 v[140:141], 0
	v_mov_b64_e32 v[74:75], 0
	v_mov_b64_e32 v[76:77], 0
	v_mov_b64_e32 v[10:11], 0
	v_mov_b64_e32 v[12:13], 0
	v_mov_b64_e32 v[66:67], 0
	v_mov_b64_e32 v[68:69], 0
	v_mov_b64_e32 v[2:3], 0
	v_mov_b64_e32 v[4:5], 0

.LBB0_470:
	v_mov_b64_e32 v[4:5], 0
	v_mov_b64_e32 v[2:3], 0
	v_mov_b64_e32 v[68:69], 0
	v_mov_b64_e32 v[66:67], 0
	v_mov_b64_e32 v[12:13], 0
	v_mov_b64_e32 v[10:11], 0
	v_mov_b64_e32 v[76:77], 0
	v_mov_b64_e32 v[74:75], 0
	v_mov_b64_e32 v[140:141], 0
	v_mov_b64_e32 v[138:139], 0
	v_mov_b64_e32 v[64:65], 0
	v_mov_b64_e32 v[62:63], 0
	v_mov_b64_e32 v[132:133], 0
	v_mov_b64_e32 v[130:131], 0
	v_mov_b64_e32 v[56:57], 0
	v_mov_b64_e32 v[54:55], 0
	v_mov_b64_e32 v[124:125], 0
	v_mov_b64_e32 v[122:123], 0
	v_mov_b64_e32 v[48:49], 0
	v_mov_b64_e32 v[46:47], 0
	v_mov_b64_e32 v[104:105], 0
	v_mov_b64_e32 v[102:103], 0
	v_mov_b64_e32 v[40:41], 0
	v_mov_b64_e32 v[38:39], 0
	v_mov_b64_e32 v[136:137], 0
	v_mov_b64_e32 v[134:135], 0
	v_mov_b64_e32 v[60:61], 0
	v_mov_b64_e32 v[58:59], 0
	v_mov_b64_e32 v[128:129], 0
	v_mov_b64_e32 v[126:127], 0
	v_mov_b64_e32 v[52:53], 0
	v_mov_b64_e32 v[50:51], 0
	v_mov_b64_e32 v[120:121], 0
	v_mov_b64_e32 v[118:119], 0
	v_mov_b64_e32 v[44:45], 0
	v_mov_b64_e32 v[42:43], 0
	v_mov_b64_e32 v[100:101], 0
	v_mov_b64_e32 v[98:99], 0
	v_mov_b64_e32 v[36:37], 0
	v_mov_b64_e32 v[34:35], 0
	v_mov_b64_e32 v[96:97], 0
	v_mov_b64_e32 v[94:95], 0
	v_mov_b64_e32 v[32:33], 0
	v_mov_b64_e32 v[30:31], 0
	v_mov_b64_e32 v[88:89], 0
	v_mov_b64_e32 v[86:87], 0
	v_mov_b64_e32 v[24:25], 0
	v_mov_b64_e32 v[22:23], 0
	v_mov_b64_e32 v[80:81], 0
	v_mov_b64_e32 v[78:79], 0
	v_mov_b64_e32 v[16:17], 0
	v_mov_b64_e32 v[14:15], 0
	v_mov_b64_e32 v[72:73], 0
	v_mov_b64_e32 v[70:71], 0
	v_mov_b64_e32 v[8:9], 0
	v_mov_b64_e32 v[6:7], 0
	v_mov_b64_e32 v[92:93], 0
	v_mov_b64_e32 v[90:91], 0
	v_mov_b64_e32 v[28:29], 0
	v_mov_b64_e32 v[26:27], 0
	v_mov_b64_e32 v[84:85], 0
	v_mov_b64_e32 v[82:83], 0
	v_mov_b64_e32 v[20:21], 0
	v_mov_b64_e32 v[18:19], 0

.LBB0_662:
	s_ashr_i32 s59, s58, 31
	s_lshl_b64 s[62:63], s[58:59], 19
	s_add_u32 s62, s10, s62
	s_addc_u32 s63, s11, s63
	s_ashr_i32 s55, s54, 31
	s_lshl_b64 s[64:65], s[54:55], 19
	s_add_u32 s64, s12, s64
	s_addc_u32 s65, s13, s65
	s_andn2_b64 vcc, exec, s[46:47]
	s_cbranch_vccnz .LBB0_752
	s_and_b64 s[74:75], s[60:61], exec
	s_cselect_b32 s29, s63, s69
	s_cselect_b32 s43, s62, s68
	s_cselect_b32 s55, s65, s71
	s_cselect_b32 s59, s64, s70
	s_add_u32 s77, s70, 0x100
	s_addc_u32 s79, s71, 0
	s_add_u32 s74, s68, 0x40080
	v_mov_b64_e32 v[34:35], 0
	s_addc_u32 s75, s69, 0
	s_mov_b32 s68, 0
	v_mov_b64_e32 v[36:37], 0
	v_mov_b64_e32 v[38:39], 0
	v_mov_b64_e32 v[40:41], 0
	v_mov_b64_e32 v[50:51], 0
	v_mov_b64_e32 v[52:53], 0
	v_mov_b64_e32 v[54:55], 0
	v_mov_b64_e32 v[56:57], 0
	v_mov_b64_e32 v[10:11], 0
	v_mov_b64_e32 v[12:13], 0
	v_mov_b64_e32 v[14:15], 0
	v_mov_b64_e32 v[16:17], 0
	v_mov_b64_e32 v[26:27], 0
	v_mov_b64_e32 v[28:29], 0
	v_mov_b64_e32 v[30:31], 0
	v_mov_b64_e32 v[32:33], 0
	v_mov_b64_e32 v[42:43], 0
	v_mov_b64_e32 v[44:45], 0
	v_mov_b64_e32 v[46:47], 0
	v_mov_b64_e32 v[48:49], 0
	v_mov_b64_e32 v[66:67], 0
	v_mov_b64_e32 v[68:69], 0
	v_mov_b64_e32 v[70:71], 0
	v_mov_b64_e32 v[72:73], 0
	v_mov_b64_e32 v[82:83], 0
	v_mov_b64_e32 v[84:85], 0
	v_mov_b64_e32 v[86:87], 0
	v_mov_b64_e32 v[88:89], 0
	v_mov_b64_e32 v[98:99], 0
	v_mov_b64_e32 v[100:101], 0
	v_mov_b64_e32 v[102:103], 0
	v_mov_b64_e32 v[104:105], 0
	v_mov_b64_e32 v[114:115], 0
	v_mov_b64_e32 v[116:117], 0
	v_mov_b64_e32 v[118:119], 0
	v_mov_b64_e32 v[120:121], 0
	v_mov_b64_e32 v[130:131], 0
	v_mov_b64_e32 v[132:133], 0
	v_mov_b64_e32 v[134:135], 0
	v_mov_b64_e32 v[136:137], 0
	v_mov_b64_e32 v[90:91], 0
	v_mov_b64_e32 v[92:93], 0
	v_mov_b64_e32 v[94:95], 0
	v_mov_b64_e32 v[96:97], 0
	v_mov_b64_e32 v[106:107], 0
	v_mov_b64_e32 v[108:109], 0
	v_mov_b64_e32 v[110:111], 0
	v_mov_b64_e32 v[112:113], 0
	v_mov_b64_e32 v[122:123], 0
	v_mov_b64_e32 v[124:125], 0
	v_mov_b64_e32 v[126:127], 0
	v_mov_b64_e32 v[128:129], 0
	v_mov_b64_e32 v[138:139], 0
	v_mov_b64_e32 v[140:141], 0
	v_mov_b64_e32 v[142:143], 0
	v_mov_b64_e32 v[144:145], 0
	v_mov_b64_e32 v[22:23], 0
	v_mov_b64_e32 v[24:25], 0
	v_mov_b64_e32 v[18:19], 0
	v_mov_b64_e32 v[20:21], 0
	v_mov_b64_e32 v[6:7], 0
	v_mov_b64_e32 v[8:9], 0
	v_mov_b64_e32 v[2:3], 0
	s_waitcnt lgkmcnt(0)
	v_mov_b64_e32 v[4:5], 0

.LBB0_752:
	v_mov_b64_e32 v[4:5], 0
	s_waitcnt lgkmcnt(0)
	v_mov_b64_e32 v[2:3], 0
	v_mov_b64_e32 v[8:9], 0
	v_mov_b64_e32 v[6:7], 0
	v_mov_b64_e32 v[20:21], 0
	v_mov_b64_e32 v[18:19], 0
	v_mov_b64_e32 v[24:25], 0
	v_mov_b64_e32 v[22:23], 0
	v_mov_b64_e32 v[144:145], 0
	v_mov_b64_e32 v[142:143], 0
	v_mov_b64_e32 v[140:141], 0
	v_mov_b64_e32 v[138:139], 0
	v_mov_b64_e32 v[128:129], 0
	v_mov_b64_e32 v[126:127], 0
	v_mov_b64_e32 v[124:125], 0
	v_mov_b64_e32 v[122:123], 0
	v_mov_b64_e32 v[112:113], 0
	v_mov_b64_e32 v[110:111], 0
	v_mov_b64_e32 v[108:109], 0
	v_mov_b64_e32 v[106:107], 0
	v_mov_b64_e32 v[96:97], 0
	v_mov_b64_e32 v[94:95], 0
	v_mov_b64_e32 v[92:93], 0
	v_mov_b64_e32 v[90:91], 0
	v_mov_b64_e32 v[136:137], 0
	v_mov_b64_e32 v[134:135], 0
	v_mov_b64_e32 v[132:133], 0
	v_mov_b64_e32 v[130:131], 0
	v_mov_b64_e32 v[120:121], 0
	v_mov_b64_e32 v[118:119], 0
	v_mov_b64_e32 v[116:117], 0
	v_mov_b64_e32 v[114:115], 0
	v_mov_b64_e32 v[104:105], 0
	v_mov_b64_e32 v[102:103], 0
	v_mov_b64_e32 v[100:101], 0
	v_mov_b64_e32 v[98:99], 0
	v_mov_b64_e32 v[88:89], 0
	v_mov_b64_e32 v[86:87], 0
	v_mov_b64_e32 v[84:85], 0
	v_mov_b64_e32 v[82:83], 0
	v_mov_b64_e32 v[72:73], 0
	v_mov_b64_e32 v[70:71], 0
	v_mov_b64_e32 v[68:69], 0
	v_mov_b64_e32 v[66:67], 0
	v_mov_b64_e32 v[48:49], 0
	v_mov_b64_e32 v[46:47], 0
	v_mov_b64_e32 v[44:45], 0
	v_mov_b64_e32 v[42:43], 0
	v_mov_b64_e32 v[32:33], 0
	v_mov_b64_e32 v[30:31], 0
	v_mov_b64_e32 v[28:29], 0
	v_mov_b64_e32 v[26:27], 0
	v_mov_b64_e32 v[16:17], 0
	v_mov_b64_e32 v[14:15], 0
	v_mov_b64_e32 v[12:13], 0
	v_mov_b64_e32 v[10:11], 0
	v_mov_b64_e32 v[56:57], 0
	v_mov_b64_e32 v[54:55], 0
	v_mov_b64_e32 v[52:53], 0
	v_mov_b64_e32 v[50:51], 0
	v_mov_b64_e32 v[40:41], 0
	v_mov_b64_e32 v[38:39], 0
	v_mov_b64_e32 v[36:37], 0
	v_mov_b64_e32 v[34:35], 0
	s_and_b64 vcc, exec, s[48:49]
	s_cbranch_vccnz .LBB0_666
	s_branch .LBB0_667

.LBB0_815:
	s_ashr_i32 s45, s44, 31
	s_lshl_b64 s[48:49], s[44:45], 19
	s_add_u32 s48, s8, s48
	s_addc_u32 s49, s10, s49
	s_ashr_i32 s43, s42, 31
	s_lshl_b64 s[50:51], s[42:43], 19
	s_add_u32 s50, s11, s50
	s_addc_u32 s51, s12, s51
	s_andn2_b64 vcc, exec, s[34:35]
	s_cbranch_vccnz .LBB0_823
	v_lshl_add_u32 v156, s52, 8, v149
	v_ashrrev_i32_e32 v157, 31, v156
	v_lshl_add_u64 v[158:159], v[156:157], 2, v[136:137]
	global_load_dword v244, v[158:159], off
	global_load_dword v245, v[158:159], off offset:64
	global_load_dword v246, v[158:159], off offset:128
	global_load_dword v247, v[158:159], off offset:192
	global_load_dword v248, v[158:159], off offset:512
	global_load_dword v249, v[158:159], off offset:576
	global_load_dword v250, v[158:159], off offset:640
	global_load_dword v251, v[158:159], off offset:704
	s_and_b64 s[60:61], s[46:47], exec
	s_cselect_b32 s43, s49, s55
	s_cselect_b32 s45, s48, s54
	s_cselect_b32 s64, s51, s59
	s_cselect_b32 s65, s50, s58
	s_add_u32 s66, s58, 0x100
	s_addc_u32 s68, s59, 0
	s_add_u32 s54, s54, 0x40080
	v_mov_b64_e32 v[34:35], 0
	v_mov_b32_e32 v1, 0x3ecc95a3
	s_addc_u32 s55, s55, 0
	s_mov_b32 s58, 0
	v_mov_b64_e32 v[36:37], 0
	v_mov_b64_e32 v[42:43], 0
	v_mov_b64_e32 v[44:45], 0
	v_mov_b64_e32 v[50:51], 0
	v_mov_b64_e32 v[52:53], 0
	v_mov_b64_e32 v[58:59], 0
	v_mov_b64_e32 v[60:61], 0
	v_mov_b64_e32 v[6:7], 0
	v_mov_b64_e32 v[8:9], 0
	v_mov_b64_e32 v[14:15], 0
	v_mov_b64_e32 v[16:17], 0
	v_mov_b64_e32 v[22:23], 0
	v_mov_b64_e32 v[24:25], 0
	v_mov_b64_e32 v[30:31], 0
	v_mov_b64_e32 v[32:33], 0
	v_mov_b64_e32 v[38:39], 0
	v_mov_b64_e32 v[40:41], 0
	v_mov_b64_e32 v[46:47], 0
	v_mov_b64_e32 v[48:49], 0
	v_mov_b64_e32 v[54:55], 0
	v_mov_b64_e32 v[56:57], 0
	v_mov_b64_e32 v[62:63], 0
	v_mov_b64_e32 v[64:65], 0
	v_mov_b64_e32 v[66:67], 0
	v_mov_b64_e32 v[68:69], 0
	v_mov_b64_e32 v[74:75], 0
	v_mov_b64_e32 v[76:77], 0
	v_mov_b64_e32 v[82:83], 0
	v_mov_b64_e32 v[84:85], 0
	v_mov_b64_e32 v[90:91], 0
	v_mov_b64_e32 v[92:93], 0
	v_mov_b64_e32 v[98:99], 0
	v_mov_b64_e32 v[100:101], 0
	v_mov_b64_e32 v[106:107], 0
	v_mov_b64_e32 v[108:109], 0
	v_mov_b64_e32 v[114:115], 0
	v_mov_b64_e32 v[116:117], 0
	v_mov_b64_e32 v[122:123], 0
	v_mov_b64_e32 v[124:125], 0
	v_mov_b64_e32 v[70:71], 0
	v_mov_b64_e32 v[72:73], 0
	v_mov_b64_e32 v[78:79], 0
	v_mov_b64_e32 v[80:81], 0
	v_mov_b64_e32 v[86:87], 0
	v_mov_b64_e32 v[88:89], 0
	v_mov_b64_e32 v[94:95], 0
	v_mov_b64_e32 v[96:97], 0
	v_mov_b64_e32 v[102:103], 0
	v_mov_b64_e32 v[104:105], 0
	v_mov_b64_e32 v[110:111], 0
	v_mov_b64_e32 v[112:113], 0
	v_mov_b64_e32 v[118:119], 0
	v_mov_b64_e32 v[120:121], 0
	v_mov_b64_e32 v[126:127], 0
	v_mov_b64_e32 v[128:129], 0
	v_mov_b64_e32 v[26:27], 0
	v_mov_b64_e32 v[28:29], 0
	v_mov_b64_e32 v[18:19], 0
	v_mov_b64_e32 v[20:21], 0
	v_mov_b64_e32 v[10:11], 0
	v_mov_b64_e32 v[12:13], 0
	v_mov_b64_e32 v[2:3], 0
	v_mov_b64_e32 v[4:5], 0

.LBB0_823:
	v_mov_b64_e32 v[4:5], 0
	v_mov_b64_e32 v[2:3], 0
	v_mov_b64_e32 v[12:13], 0
	v_mov_b64_e32 v[10:11], 0
	v_mov_b64_e32 v[20:21], 0
	v_mov_b64_e32 v[18:19], 0
	v_mov_b64_e32 v[28:29], 0
	v_mov_b64_e32 v[26:27], 0
	v_mov_b64_e32 v[128:129], 0
	v_mov_b64_e32 v[126:127], 0
	v_mov_b64_e32 v[120:121], 0
	v_mov_b64_e32 v[118:119], 0
	v_mov_b64_e32 v[112:113], 0
	v_mov_b64_e32 v[110:111], 0
	v_mov_b64_e32 v[104:105], 0
	v_mov_b64_e32 v[102:103], 0
	v_mov_b64_e32 v[96:97], 0
	v_mov_b64_e32 v[94:95], 0
	v_mov_b64_e32 v[88:89], 0
	v_mov_b64_e32 v[86:87], 0
	v_mov_b64_e32 v[80:81], 0
	v_mov_b64_e32 v[78:79], 0
	v_mov_b64_e32 v[72:73], 0
	v_mov_b64_e32 v[70:71], 0
	v_mov_b64_e32 v[124:125], 0
	v_mov_b64_e32 v[122:123], 0
	v_mov_b64_e32 v[116:117], 0
	v_mov_b64_e32 v[114:115], 0
	v_mov_b64_e32 v[108:109], 0
	v_mov_b64_e32 v[106:107], 0
	v_mov_b64_e32 v[100:101], 0
	v_mov_b64_e32 v[98:99], 0
	v_mov_b64_e32 v[92:93], 0
	v_mov_b64_e32 v[90:91], 0
	v_mov_b64_e32 v[84:85], 0
	v_mov_b64_e32 v[82:83], 0
	v_mov_b64_e32 v[76:77], 0
	v_mov_b64_e32 v[74:75], 0
	v_mov_b64_e32 v[68:69], 0
	v_mov_b64_e32 v[66:67], 0
	v_mov_b64_e32 v[64:65], 0
	v_mov_b64_e32 v[62:63], 0
	v_mov_b64_e32 v[56:57], 0
	v_mov_b64_e32 v[54:55], 0
	v_mov_b64_e32 v[48:49], 0
	v_mov_b64_e32 v[46:47], 0
	v_mov_b64_e32 v[40:41], 0
	v_mov_b64_e32 v[38:39], 0
	v_mov_b64_e32 v[32:33], 0
	v_mov_b64_e32 v[30:31], 0
	v_mov_b64_e32 v[24:25], 0
	v_mov_b64_e32 v[22:23], 0
	v_mov_b64_e32 v[16:17], 0
	v_mov_b64_e32 v[14:15], 0
	v_mov_b64_e32 v[8:9], 0
	v_mov_b64_e32 v[6:7], 0
	v_mov_b64_e32 v[60:61], 0
	v_mov_b64_e32 v[58:59], 0
	v_mov_b64_e32 v[52:53], 0
	v_mov_b64_e32 v[50:51], 0
	v_mov_b64_e32 v[44:45], 0
	v_mov_b64_e32 v[42:43], 0
	v_mov_b64_e32 v[36:37], 0
	v_mov_b64_e32 v[34:35], 0
	s_and_b64 vcc, exec, s[36:37]
	s_cbranch_vccnz .LBB0_819
	s_branch .LBB0_820

.LBB0_840:
	s_ashr_i32 s43, s42, 31
	s_lshl_b64 s[46:47], s[42:43], 18
	s_add_u32 s46, s8, s46
	s_addc_u32 s47, s10, s47
	s_ashr_i32 s41, s40, 31
	s_lshl_b64 s[48:49], s[40:41], 18
	s_add_u32 s48, s11, s48
	s_addc_u32 s49, s12, s49
	s_andn2_b64 vcc, exec, s[34:35]
	s_cbranch_vccnz .LBB0_848
	v_lshl_add_u32 v2, s50, 8, v195
	v_ashrrev_i32_e32 v3, 31, v2
	v_lshl_add_u64 v[4:5], v[2:3], 2, v[180:181]
	global_load_dword v244, v[4:5], off
	global_load_dword v245, v[4:5], off offset:64
	global_load_dword v246, v[4:5], off offset:128
	global_load_dword v247, v[4:5], off offset:192
	global_load_dword v248, v[4:5], off offset:512
	global_load_dword v249, v[4:5], off offset:576
	global_load_dword v250, v[4:5], off offset:640
	global_load_dword v251, v[4:5], off offset:704
	s_and_b64 s[58:59], s[44:45], exec
	s_cselect_b32 s41, s47, s53
	s_cselect_b32 s43, s46, s52
	s_cselect_b32 s62, s49, s55
	s_cselect_b32 s63, s48, s54
	s_add_u32 s64, s54, 0x100
	s_addc_u32 s65, s55, 0
	s_add_u32 s52, s52, 0x20080
	v_mov_b64_e32 v[66:67], 0
	v_mov_b32_e32 v1, 0x3ecc95a3
	s_addc_u32 s53, s53, 0
	s_mov_b32 s54, 0
	v_mov_b64_e32 v[68:69], 0
	v_mov_b64_e32 v[74:75], 0
	v_mov_b64_e32 v[76:77], 0
	v_mov_b64_e32 v[82:83], 0
	v_mov_b64_e32 v[84:85], 0
	v_mov_b64_e32 v[90:91], 0
	v_mov_b64_e32 v[92:93], 0
	v_mov_b64_e32 v[38:39], 0
	v_mov_b64_e32 v[40:41], 0
	v_mov_b64_e32 v[46:47], 0
	v_mov_b64_e32 v[48:49], 0
	v_mov_b64_e32 v[54:55], 0
	v_mov_b64_e32 v[56:57], 0
	v_mov_b64_e32 v[62:63], 0
	v_mov_b64_e32 v[64:65], 0
	v_mov_b64_e32 v[70:71], 0
	v_mov_b64_e32 v[72:73], 0
	v_mov_b64_e32 v[78:79], 0
	v_mov_b64_e32 v[80:81], 0
	v_mov_b64_e32 v[86:87], 0
	v_mov_b64_e32 v[88:89], 0
	v_mov_b64_e32 v[94:95], 0
	v_mov_b64_e32 v[96:97], 0
	v_mov_b64_e32 v[98:99], 0
	v_mov_b64_e32 v[100:101], 0
	v_mov_b64_e32 v[106:107], 0
	v_mov_b64_e32 v[108:109], 0
	v_mov_b64_e32 v[114:115], 0
	v_mov_b64_e32 v[116:117], 0
	v_mov_b64_e32 v[122:123], 0
	v_mov_b64_e32 v[124:125], 0
	v_mov_b64_e32 v[130:131], 0
	v_mov_b64_e32 v[132:133], 0
	v_mov_b64_e32 v[138:139], 0
	v_mov_b64_e32 v[140:141], 0
	v_mov_b64_e32 v[146:147], 0
	v_mov_b64_e32 v[148:149], 0
	v_mov_b64_e32 v[154:155], 0
	v_mov_b64_e32 v[156:157], 0
	v_mov_b64_e32 v[102:103], 0
	v_mov_b64_e32 v[104:105], 0
	v_mov_b64_e32 v[110:111], 0
	v_mov_b64_e32 v[112:113], 0
	v_mov_b64_e32 v[118:119], 0
	v_mov_b64_e32 v[120:121], 0
	v_mov_b64_e32 v[126:127], 0
	v_mov_b64_e32 v[128:129], 0
	v_mov_b64_e32 v[134:135], 0
	v_mov_b64_e32 v[136:137], 0
	v_mov_b64_e32 v[142:143], 0
	v_mov_b64_e32 v[144:145], 0
	v_mov_b64_e32 v[150:151], 0
	v_mov_b64_e32 v[152:153], 0
	v_mov_b64_e32 v[158:159], 0
	v_mov_b64_e32 v[160:161], 0
	v_mov_b64_e32 v[58:59], 0
	v_mov_b64_e32 v[60:61], 0
	v_mov_b64_e32 v[50:51], 0
	v_mov_b64_e32 v[52:53], 0
	v_mov_b64_e32 v[42:43], 0
	v_mov_b64_e32 v[44:45], 0
	v_mov_b64_e32 v[34:35], 0
	v_mov_b64_e32 v[36:37], 0

.LBB0_848:
	v_mov_b64_e32 v[36:37], 0
	v_mov_b64_e32 v[34:35], 0
	v_mov_b64_e32 v[44:45], 0
	v_mov_b64_e32 v[42:43], 0
	v_mov_b64_e32 v[52:53], 0
	v_mov_b64_e32 v[50:51], 0
	v_mov_b64_e32 v[60:61], 0
	v_mov_b64_e32 v[58:59], 0
	v_mov_b64_e32 v[160:161], 0
	v_mov_b64_e32 v[158:159], 0
	v_mov_b64_e32 v[152:153], 0
	v_mov_b64_e32 v[150:151], 0
	v_mov_b64_e32 v[144:145], 0
	v_mov_b64_e32 v[142:143], 0
	v_mov_b64_e32 v[136:137], 0
	v_mov_b64_e32 v[134:135], 0
	v_mov_b64_e32 v[128:129], 0
	v_mov_b64_e32 v[126:127], 0
	v_mov_b64_e32 v[120:121], 0
	v_mov_b64_e32 v[118:119], 0
	v_mov_b64_e32 v[112:113], 0
	v_mov_b64_e32 v[110:111], 0
	v_mov_b64_e32 v[104:105], 0
	v_mov_b64_e32 v[102:103], 0
	v_mov_b64_e32 v[156:157], 0
	v_mov_b64_e32 v[154:155], 0
	v_mov_b64_e32 v[148:149], 0
	v_mov_b64_e32 v[146:147], 0
	v_mov_b64_e32 v[140:141], 0
	v_mov_b64_e32 v[138:139], 0
	v_mov_b64_e32 v[132:133], 0
	v_mov_b64_e32 v[130:131], 0
	v_mov_b64_e32 v[124:125], 0
	v_mov_b64_e32 v[122:123], 0
	v_mov_b64_e32 v[116:117], 0
	v_mov_b64_e32 v[114:115], 0
	v_mov_b64_e32 v[108:109], 0
	v_mov_b64_e32 v[106:107], 0
	v_mov_b64_e32 v[100:101], 0
	v_mov_b64_e32 v[98:99], 0
	v_mov_b64_e32 v[96:97], 0
	v_mov_b64_e32 v[94:95], 0
	v_mov_b64_e32 v[88:89], 0
	v_mov_b64_e32 v[86:87], 0
	v_mov_b64_e32 v[80:81], 0
	v_mov_b64_e32 v[78:79], 0
	v_mov_b64_e32 v[72:73], 0
	v_mov_b64_e32 v[70:71], 0
	v_mov_b64_e32 v[64:65], 0
	v_mov_b64_e32 v[62:63], 0
	v_mov_b64_e32 v[56:57], 0
	v_mov_b64_e32 v[54:55], 0
	v_mov_b64_e32 v[48:49], 0
	v_mov_b64_e32 v[46:47], 0
	v_mov_b64_e32 v[40:41], 0
	v_mov_b64_e32 v[38:39], 0
	v_mov_b64_e32 v[92:93], 0
	v_mov_b64_e32 v[90:91], 0
	v_mov_b64_e32 v[84:85], 0
	v_mov_b64_e32 v[82:83], 0
	v_mov_b64_e32 v[76:77], 0
	v_mov_b64_e32 v[74:75], 0
	v_mov_b64_e32 v[68:69], 0
	v_mov_b64_e32 v[66:67], 0
	s_and_b64 vcc, exec, s[36:37]
	s_cbranch_vccnz .LBB0_844
	s_branch .LBB0_845

.LBB0_923:
	s_add_u32 s73, s60, 0x100
	v_mov_b64_e32 v[66:67], 0
	v_mov_b32_e32 v1, 0x3ecc95a3
	s_addc_u32 s74, s61, 0
	s_mov_b32 s62, 0
	v_mov_b64_e32 v[68:69], 0
	v_mov_b64_e32 v[70:71], 0
	v_mov_b64_e32 v[72:73], 0
	v_mov_b64_e32 v[82:83], 0
	v_mov_b64_e32 v[84:85], 0
	v_mov_b64_e32 v[86:87], 0
	v_mov_b64_e32 v[88:89], 0
	v_mov_b64_e32 v[42:43], 0
	v_mov_b64_e32 v[44:45], 0
	v_mov_b64_e32 v[46:47], 0
	v_mov_b64_e32 v[48:49], 0
	v_mov_b64_e32 v[58:59], 0
	v_mov_b64_e32 v[60:61], 0
	v_mov_b64_e32 v[62:63], 0
	v_mov_b64_e32 v[64:65], 0
	v_mov_b64_e32 v[74:75], 0
	v_mov_b64_e32 v[76:77], 0
	v_mov_b64_e32 v[78:79], 0
	v_mov_b64_e32 v[80:81], 0
	v_mov_b64_e32 v[90:91], 0
	v_mov_b64_e32 v[92:93], 0
	v_mov_b64_e32 v[94:95], 0
	v_mov_b64_e32 v[96:97], 0
	v_mov_b64_e32 v[98:99], 0
	v_mov_b64_e32 v[100:101], 0
	v_mov_b64_e32 v[102:103], 0
	v_mov_b64_e32 v[104:105], 0
	v_mov_b64_e32 v[114:115], 0
	v_mov_b64_e32 v[116:117], 0
	v_mov_b64_e32 v[118:119], 0
	v_mov_b64_e32 v[120:121], 0
	v_mov_b64_e32 v[130:131], 0
	v_mov_b64_e32 v[132:133], 0
	v_mov_b64_e32 v[134:135], 0
	v_mov_b64_e32 v[136:137], 0
	v_mov_b64_e32 v[146:147], 0
	v_mov_b64_e32 v[148:149], 0
	v_mov_b64_e32 v[150:151], 0
	v_mov_b64_e32 v[152:153], 0
	v_mov_b64_e32 v[106:107], 0
	v_mov_b64_e32 v[108:109], 0
	v_mov_b64_e32 v[110:111], 0
	v_mov_b64_e32 v[112:113], 0
	v_mov_b64_e32 v[122:123], 0
	v_mov_b64_e32 v[124:125], 0
	v_mov_b64_e32 v[126:127], 0
	v_mov_b64_e32 v[128:129], 0
	v_mov_b64_e32 v[138:139], 0
	v_mov_b64_e32 v[140:141], 0
	v_mov_b64_e32 v[142:143], 0
	v_mov_b64_e32 v[144:145], 0
	v_mov_b64_e32 v[154:155], 0
	v_mov_b64_e32 v[156:157], 0
	v_mov_b64_e32 v[158:159], 0
	v_mov_b64_e32 v[160:161], 0
	v_mov_b64_e32 v[54:55], 0
	v_mov_b64_e32 v[56:57], 0
	v_mov_b64_e32 v[50:51], 0
	v_mov_b64_e32 v[52:53], 0
	v_mov_b64_e32 v[38:39], 0
	v_mov_b64_e32 v[40:41], 0
	v_mov_b64_e32 v[34:35], 0
	v_mov_b64_e32 v[36:37], 0

.LBB0_950:
	v_mov_b64_e32 v[36:37], 0
	v_mov_b64_e32 v[34:35], 0
	v_mov_b64_e32 v[40:41], 0
	v_mov_b64_e32 v[38:39], 0
	v_mov_b64_e32 v[52:53], 0
	v_mov_b64_e32 v[50:51], 0
	v_mov_b64_e32 v[56:57], 0
	v_mov_b64_e32 v[54:55], 0
	v_mov_b64_e32 v[160:161], 0
	v_mov_b64_e32 v[158:159], 0
	v_mov_b64_e32 v[156:157], 0
	v_mov_b64_e32 v[154:155], 0
	v_mov_b64_e32 v[144:145], 0
	v_mov_b64_e32 v[142:143], 0
	v_mov_b64_e32 v[140:141], 0
	v_mov_b64_e32 v[138:139], 0
	v_mov_b64_e32 v[128:129], 0
	v_mov_b64_e32 v[126:127], 0
	v_mov_b64_e32 v[124:125], 0
	v_mov_b64_e32 v[122:123], 0
	v_mov_b64_e32 v[112:113], 0
	v_mov_b64_e32 v[110:111], 0
	v_mov_b64_e32 v[108:109], 0
	v_mov_b64_e32 v[106:107], 0
	v_mov_b64_e32 v[152:153], 0
	v_mov_b64_e32 v[150:151], 0
	v_mov_b64_e32 v[148:149], 0
	v_mov_b64_e32 v[146:147], 0
	v_mov_b64_e32 v[136:137], 0
	v_mov_b64_e32 v[134:135], 0
	v_mov_b64_e32 v[132:133], 0
	v_mov_b64_e32 v[130:131], 0
	v_mov_b64_e32 v[120:121], 0
	v_mov_b64_e32 v[118:119], 0
	v_mov_b64_e32 v[116:117], 0
	v_mov_b64_e32 v[114:115], 0
	v_mov_b64_e32 v[104:105], 0
	v_mov_b64_e32 v[102:103], 0
	v_mov_b64_e32 v[100:101], 0
	v_mov_b64_e32 v[98:99], 0
	v_mov_b64_e32 v[96:97], 0
	v_mov_b64_e32 v[94:95], 0
	v_mov_b64_e32 v[92:93], 0
	v_mov_b64_e32 v[90:91], 0
	v_mov_b64_e32 v[80:81], 0
	v_mov_b64_e32 v[78:79], 0
	v_mov_b64_e32 v[76:77], 0
	v_mov_b64_e32 v[74:75], 0
	v_mov_b64_e32 v[64:65], 0
	v_mov_b64_e32 v[62:63], 0
	v_mov_b64_e32 v[60:61], 0
	v_mov_b64_e32 v[58:59], 0
	v_mov_b64_e32 v[48:49], 0
	v_mov_b64_e32 v[46:47], 0
	v_mov_b64_e32 v[44:45], 0
	v_mov_b64_e32 v[42:43], 0
	v_mov_b64_e32 v[88:89], 0
	v_mov_b64_e32 v[86:87], 0
	v_mov_b64_e32 v[84:85], 0
	v_mov_b64_e32 v[82:83], 0
	v_mov_b64_e32 v[72:73], 0
	v_mov_b64_e32 v[70:71], 0
	v_mov_b64_e32 v[68:69], 0
	v_mov_b64_e32 v[66:67], 0
	s_and_b64 vcc, exec, s[46:47]
	s_cbranch_vccnz .LBB0_926
	s_branch .LBB0_927

.LBB0_1014:
	s_ashr_i32 s27, s26, 31
	s_lshl_b64 s[0:1], s[26:27], 18
	s_add_u32 s30, s90, s0
	s_addc_u32 s31, s91, s1
	s_ashr_i32 s65, s64, 31
	s_lshl_b64 s[0:1], s[64:65], 18
	s_add_u32 s34, s76, s0
	s_addc_u32 s35, s77, s1
	s_andn2_b64 vcc, exec, s[50:51]
	s_cbranch_vccnz .LBB0_1078
	v_lshl_add_u32 v2, s36, 8, v220
	v_ashrrev_i32_e32 v3, 31, v2
	v_lshl_add_u64 v[4:5], v[2:3], 2, v[186:187]
	global_load_dword v172, v[4:5], off
	global_load_dword v173, v[4:5], off offset:64
	global_load_dword v174, v[4:5], off offset:128
	global_load_dword v175, v[4:5], off offset:192
	global_load_dword v176, v[4:5], off offset:512
	global_load_dword v177, v[4:5], off offset:576
	global_load_dword v223, v[4:5], off offset:640
	global_load_dword v232, v[4:5], off offset:704
	s_and_b64 s[0:1], s[28:29], exec
	s_cselect_b32 s0, s31, s39
	s_cselect_b32 s1, s30, s38
	s_cselect_b32 s8, s35, s41
	s_cselect_b32 s11, s34, s40
	s_add_u32 s16, s40, 0x100
	s_addc_u32 s19, s41, 0
	s_add_u32 s38, s38, 0x20080
	v_mov_b64_e32 v[114:115], 0
	v_mov_b32_e32 v1, 0x3ecc95a3
	s_addc_u32 s39, s39, 0
	s_mov_b32 s37, 0
	v_mov_b64_e32 v[116:117], 0
	v_mov_b64_e32 v[118:119], 0
	v_mov_b64_e32 v[120:121], 0
	v_mov_b64_e32 v[122:123], 0
	v_mov_b64_e32 v[124:125], 0
	v_mov_b64_e32 v[126:127], 0
	v_mov_b64_e32 v[128:129], 0
	v_mov_b64_e32 v[34:35], 0
	v_mov_b64_e32 v[36:37], 0
	v_mov_b64_e32 v[38:39], 0
	v_mov_b64_e32 v[40:41], 0
	v_mov_b64_e32 v[42:43], 0
	v_mov_b64_e32 v[44:45], 0
	v_mov_b64_e32 v[46:47], 0
	v_mov_b64_e32 v[48:49], 0
	v_mov_b64_e32 v[50:51], 0
	v_mov_b64_e32 v[52:53], 0
	v_mov_b64_e32 v[54:55], 0
	v_mov_b64_e32 v[56:57], 0
	v_mov_b64_e32 v[58:59], 0
	v_mov_b64_e32 v[60:61], 0
	v_mov_b64_e32 v[62:63], 0
	v_mov_b64_e32 v[64:65], 0
	v_mov_b64_e32 v[130:131], 0
	v_mov_b64_e32 v[132:133], 0
	v_mov_b64_e32 v[134:135], 0
	v_mov_b64_e32 v[136:137], 0
	v_mov_b64_e32 v[138:139], 0
	v_mov_b64_e32 v[140:141], 0
	v_mov_b64_e32 v[142:143], 0
	v_mov_b64_e32 v[144:145], 0
	v_mov_b64_e32 v[146:147], 0
	v_mov_b64_e32 v[148:149], 0
	v_mov_b64_e32 v[150:151], 0
	v_mov_b64_e32 v[152:153], 0
	v_mov_b64_e32 v[154:155], 0
	v_mov_b64_e32 v[156:157], 0
	v_mov_b64_e32 v[158:159], 0
	v_mov_b64_e32 v[160:161], 0
	v_mov_b64_e32 v[66:67], 0
	v_mov_b64_e32 v[68:69], 0
	v_mov_b64_e32 v[70:71], 0
	v_mov_b64_e32 v[72:73], 0
	v_mov_b64_e32 v[74:75], 0
	v_mov_b64_e32 v[76:77], 0
	v_mov_b64_e32 v[78:79], 0
	v_mov_b64_e32 v[80:81], 0
	v_mov_b64_e32 v[82:83], 0
	v_mov_b64_e32 v[84:85], 0
	v_mov_b64_e32 v[86:87], 0
	v_mov_b64_e32 v[88:89], 0
	v_mov_b64_e32 v[90:91], 0
	v_mov_b64_e32 v[92:93], 0
	v_mov_b64_e32 v[94:95], 0
	v_mov_b64_e32 v[96:97], 0
	v_mov_b64_e32 v[110:111], 0
	v_mov_b64_e32 v[112:113], 0
	v_mov_b64_e32 v[106:107], 0
	v_mov_b64_e32 v[108:109], 0
	v_mov_b64_e32 v[102:103], 0
	v_mov_b64_e32 v[104:105], 0
	v_mov_b64_e32 v[98:99], 0
	v_mov_b64_e32 v[100:101], 0

.LBB0_1078:
	v_mov_b64_e32 v[100:101], 0
	v_mov_b64_e32 v[98:99], 0
	v_mov_b64_e32 v[104:105], 0
	v_mov_b64_e32 v[102:103], 0
	v_mov_b64_e32 v[108:109], 0
	v_mov_b64_e32 v[106:107], 0
	v_mov_b64_e32 v[112:113], 0
	v_mov_b64_e32 v[110:111], 0
	v_mov_b64_e32 v[96:97], 0
	v_mov_b64_e32 v[94:95], 0
	v_mov_b64_e32 v[92:93], 0
	v_mov_b64_e32 v[90:91], 0
	v_mov_b64_e32 v[88:89], 0
	v_mov_b64_e32 v[86:87], 0
	v_mov_b64_e32 v[84:85], 0
	v_mov_b64_e32 v[82:83], 0
	v_mov_b64_e32 v[80:81], 0
	v_mov_b64_e32 v[78:79], 0
	v_mov_b64_e32 v[76:77], 0
	v_mov_b64_e32 v[74:75], 0
	v_mov_b64_e32 v[72:73], 0
	v_mov_b64_e32 v[70:71], 0
	v_mov_b64_e32 v[68:69], 0
	v_mov_b64_e32 v[66:67], 0
	v_mov_b64_e32 v[160:161], 0
	v_mov_b64_e32 v[158:159], 0
	v_mov_b64_e32 v[156:157], 0
	v_mov_b64_e32 v[154:155], 0
	v_mov_b64_e32 v[152:153], 0
	v_mov_b64_e32 v[150:151], 0
	v_mov_b64_e32 v[148:149], 0
	v_mov_b64_e32 v[146:147], 0
	v_mov_b64_e32 v[144:145], 0
	v_mov_b64_e32 v[142:143], 0
	v_mov_b64_e32 v[140:141], 0
	v_mov_b64_e32 v[138:139], 0
	v_mov_b64_e32 v[136:137], 0
	v_mov_b64_e32 v[134:135], 0
	v_mov_b64_e32 v[132:133], 0
	v_mov_b64_e32 v[130:131], 0
	v_mov_b64_e32 v[64:65], 0
	v_mov_b64_e32 v[62:63], 0
	v_mov_b64_e32 v[60:61], 0
	v_mov_b64_e32 v[58:59], 0
	v_mov_b64_e32 v[56:57], 0
	v_mov_b64_e32 v[54:55], 0
	v_mov_b64_e32 v[52:53], 0
	v_mov_b64_e32 v[50:51], 0
	v_mov_b64_e32 v[48:49], 0
	v_mov_b64_e32 v[46:47], 0
	v_mov_b64_e32 v[44:45], 0
	v_mov_b64_e32 v[42:43], 0
	v_mov_b64_e32 v[40:41], 0
	v_mov_b64_e32 v[38:39], 0
	v_mov_b64_e32 v[36:37], 0
	v_mov_b64_e32 v[34:35], 0
	v_mov_b64_e32 v[128:129], 0
	v_mov_b64_e32 v[126:127], 0
	v_mov_b64_e32 v[124:125], 0
	v_mov_b64_e32 v[122:123], 0
	v_mov_b64_e32 v[120:121], 0
	v_mov_b64_e32 v[118:119], 0
	v_mov_b64_e32 v[116:117], 0
	v_mov_b64_e32 v[114:115], 0
	s_and_b64 vcc, exec, s[52:53]
	s_cbranch_vccnz .LBB0_1018
	s_branch .LBB0_1019

.LBB0_1436:
	s_ashr_i32 s43, s42, 31
	s_lshl_b64 s[46:47], s[42:43], 19
	s_add_u32 s46, s11, s46
	s_addc_u32 s47, s12, s47
	s_ashr_i32 s41, s40, 31
	s_lshl_b64 s[48:49], s[40:41], 19
	s_add_u32 s48, s13, s48
	s_addc_u32 s49, s14, s49
	s_andn2_b64 vcc, exec, s[30:31]
	s_cbranch_vccnz .LBB0_1444
	s_and_b64 s[58:59], s[44:45], exec
	s_cselect_b32 s41, s47, s53
	s_cselect_b32 s43, s46, s52
	s_cselect_b32 s62, s49, s55
	s_cselect_b32 s63, s48, s54
	s_add_u32 s64, s54, 0x100
	s_addc_u32 s65, s55, 0
	s_add_u32 s52, s52, 0x40080
	v_mov_b64_e32 v[34:35], 0
	v_mov_b32_e32 v1, 0x3ecc95a3
	s_addc_u32 s53, s53, 0
	s_mov_b32 s54, 0
	v_mov_b64_e32 v[36:37], 0
	v_mov_b64_e32 v[38:39], 0
	v_mov_b64_e32 v[40:41], 0
	v_mov_b64_e32 v[50:51], 0
	v_mov_b64_e32 v[52:53], 0
	v_mov_b64_e32 v[54:55], 0
	v_mov_b64_e32 v[56:57], 0
	v_mov_b64_e32 v[10:11], 0
	v_mov_b64_e32 v[12:13], 0
	v_mov_b64_e32 v[14:15], 0
	v_mov_b64_e32 v[16:17], 0
	v_mov_b64_e32 v[26:27], 0
	v_mov_b64_e32 v[28:29], 0
	v_mov_b64_e32 v[30:31], 0
	v_mov_b64_e32 v[32:33], 0
	v_mov_b64_e32 v[42:43], 0
	v_mov_b64_e32 v[44:45], 0
	v_mov_b64_e32 v[46:47], 0
	v_mov_b64_e32 v[48:49], 0
	v_mov_b64_e32 v[58:59], 0
	v_mov_b64_e32 v[60:61], 0
	v_mov_b64_e32 v[62:63], 0
	v_mov_b64_e32 v[64:65], 0
	v_mov_b64_e32 v[66:67], 0
	v_mov_b64_e32 v[68:69], 0
	v_mov_b64_e32 v[70:71], 0
	v_mov_b64_e32 v[72:73], 0
	v_mov_b64_e32 v[82:83], 0
	v_mov_b64_e32 v[84:85], 0
	v_mov_b64_e32 v[86:87], 0
	v_mov_b64_e32 v[88:89], 0
	v_mov_b64_e32 v[98:99], 0
	v_mov_b64_e32 v[100:101], 0
	v_mov_b64_e32 v[102:103], 0
	v_mov_b64_e32 v[104:105], 0
	v_mov_b64_e32 v[114:115], 0
	v_mov_b64_e32 v[116:117], 0
	v_mov_b64_e32 v[118:119], 0
	v_mov_b64_e32 v[120:121], 0
	v_mov_b64_e32 v[74:75], 0
	v_mov_b64_e32 v[76:77], 0
	v_mov_b64_e32 v[78:79], 0
	v_mov_b64_e32 v[80:81], 0
	v_mov_b64_e32 v[90:91], 0
	v_mov_b64_e32 v[92:93], 0
	v_mov_b64_e32 v[94:95], 0
	v_mov_b64_e32 v[96:97], 0
	v_mov_b64_e32 v[106:107], 0
	v_mov_b64_e32 v[108:109], 0
	v_mov_b64_e32 v[110:111], 0
	v_mov_b64_e32 v[112:113], 0
	v_mov_b64_e32 v[122:123], 0
	v_mov_b64_e32 v[124:125], 0
	v_mov_b64_e32 v[126:127], 0
	v_mov_b64_e32 v[128:129], 0
	v_mov_b64_e32 v[22:23], 0
	v_mov_b64_e32 v[24:25], 0
	v_mov_b64_e32 v[18:19], 0
	v_mov_b64_e32 v[20:21], 0
	v_mov_b64_e32 v[6:7], 0
	v_mov_b64_e32 v[8:9], 0
	v_mov_b64_e32 v[2:3], 0
	v_mov_b64_e32 v[4:5], 0

.LBB0_1689:
	s_andn2_b64 vcc, exec, s[42:43]
	s_cbranch_vccnz .LBB0_1700
	s_lshl_b32 s51, s52, 8
	v_add_u32_e32 v2, s51, v169
	v_add_u32_e32 v4, s51, v205
	s_bitset1_b32 s51, 7
	v_add_u32_e32 v6, s51, v169
	v_add_u32_e32 v8, s51, v205
	v_ashrrev_i32_e32 v3, 31, v2
	v_ashrrev_i32_e32 v5, 31, v4
	v_ashrrev_i32_e32 v7, 31, v6
	v_ashrrev_i32_e32 v9, 31, v8
	v_mov_b32_e32 v181, v167
	v_mov_b32_e32 v183, v167
	s_add_u32 s51, s64, 0x100
	v_mov_b64_e32 v[34:35], 0
	v_lshl_add_u64 v[184:185], v[2:3], 2, s[30:31]
	v_lshl_add_u64 v[186:187], v[4:5], 2, s[30:31]
	v_lshl_add_u64 v[188:189], v[6:7], 2, s[30:31]
	v_lshl_add_u64 v[190:191], v[8:9], 2, s[30:31]
	s_addc_u32 s53, s65, 0
	s_and_b64 vcc, exec, s[62:63]
	s_cbranch_vccz .Lnolist_15
	global_load_dword v184, v[184:185], off
	global_load_dword v186, v[186:187], off
	global_load_dword v188, v[188:189], off
	global_load_dword v190, v[190:191], off
.Lnolist_15:
	v_lshl_add_u64 v[192:193], s[40:41], 0, v[182:183]
	v_lshl_add_u64 v[194:195], s[40:41], 0, v[180:181]
	s_mov_b32 s91, 0
	s_mov_b64 s[70:71], 0
	v_mov_b64_e32 v[36:37], 0
	v_mov_b64_e32 v[42:43], 0
	v_mov_b64_e32 v[44:45], 0
	v_mov_b64_e32 v[50:51], 0
	v_mov_b64_e32 v[52:53], 0
	v_mov_b64_e32 v[58:59], 0
	v_mov_b64_e32 v[60:61], 0
	v_mov_b64_e32 v[66:67], 0
	v_mov_b64_e32 v[68:69], 0
	v_mov_b64_e32 v[74:75], 0
	v_mov_b64_e32 v[76:77], 0
	v_mov_b64_e32 v[82:83], 0
	v_mov_b64_e32 v[84:85], 0
	v_mov_b64_e32 v[90:91], 0
	v_mov_b64_e32 v[92:93], 0
	v_mov_b64_e32 v[38:39], 0
	v_mov_b64_e32 v[40:41], 0
	v_mov_b64_e32 v[46:47], 0
	v_mov_b64_e32 v[48:49], 0
	v_mov_b64_e32 v[54:55], 0
	v_mov_b64_e32 v[56:57], 0
	v_mov_b64_e32 v[62:63], 0
	v_mov_b64_e32 v[64:65], 0
	v_mov_b64_e32 v[70:71], 0
	v_mov_b64_e32 v[72:73], 0
	v_mov_b64_e32 v[78:79], 0
	v_mov_b64_e32 v[80:81], 0
	v_mov_b64_e32 v[86:87], 0
	v_mov_b64_e32 v[88:89], 0
	v_mov_b64_e32 v[94:95], 0
	v_mov_b64_e32 v[96:97], 0
	v_mov_b64_e32 v[98:99], 0
	v_mov_b64_e32 v[100:101], 0
	v_mov_b64_e32 v[106:107], 0
	v_mov_b64_e32 v[108:109], 0
	v_mov_b64_e32 v[114:115], 0
	v_mov_b64_e32 v[116:117], 0
	v_mov_b64_e32 v[122:123], 0
	v_mov_b64_e32 v[124:125], 0
	v_mov_b64_e32 v[130:131], 0
	v_mov_b64_e32 v[132:133], 0
	v_mov_b64_e32 v[138:139], 0
	v_mov_b64_e32 v[140:141], 0
	v_mov_b64_e32 v[146:147], 0
	v_mov_b64_e32 v[148:149], 0
	v_mov_b64_e32 v[158:159], 0
	v_mov_b64_e32 v[160:161], 0
	v_mov_b64_e32 v[102:103], 0
	v_mov_b64_e32 v[104:105], 0
	v_mov_b64_e32 v[110:111], 0
	v_mov_b64_e32 v[112:113], 0
	v_mov_b64_e32 v[118:119], 0
	v_mov_b64_e32 v[120:121], 0
	v_mov_b64_e32 v[126:127], 0
	v_mov_b64_e32 v[128:129], 0
	v_mov_b64_e32 v[134:135], 0
	v_mov_b64_e32 v[136:137], 0
	v_mov_b64_e32 v[142:143], 0
	v_mov_b64_e32 v[144:145], 0
	v_mov_b64_e32 v[150:151], 0
	v_mov_b64_e32 v[152:153], 0
	v_mov_b64_e32 v[154:155], 0
	v_mov_b64_e32 v[156:157], 0

.LBB0_1700:
	v_mov_b64_e32 v[156:157], 0
	v_mov_b64_e32 v[154:155], 0
	v_mov_b64_e32 v[152:153], 0
	v_mov_b64_e32 v[150:151], 0
	v_mov_b64_e32 v[144:145], 0
	v_mov_b64_e32 v[142:143], 0
	v_mov_b64_e32 v[136:137], 0
	v_mov_b64_e32 v[134:135], 0
	v_mov_b64_e32 v[128:129], 0
	v_mov_b64_e32 v[126:127], 0
	v_mov_b64_e32 v[120:121], 0
	v_mov_b64_e32 v[118:119], 0
	v_mov_b64_e32 v[112:113], 0
	v_mov_b64_e32 v[110:111], 0
	v_mov_b64_e32 v[104:105], 0
	v_mov_b64_e32 v[102:103], 0
	v_mov_b64_e32 v[160:161], 0
	v_mov_b64_e32 v[158:159], 0
	v_mov_b64_e32 v[148:149], 0
	v_mov_b64_e32 v[146:147], 0
	v_mov_b64_e32 v[140:141], 0
	v_mov_b64_e32 v[138:139], 0
	v_mov_b64_e32 v[132:133], 0
	v_mov_b64_e32 v[130:131], 0
	v_mov_b64_e32 v[124:125], 0
	v_mov_b64_e32 v[122:123], 0
	v_mov_b64_e32 v[116:117], 0
	v_mov_b64_e32 v[114:115], 0
	v_mov_b64_e32 v[108:109], 0
	v_mov_b64_e32 v[106:107], 0
	v_mov_b64_e32 v[100:101], 0
	v_mov_b64_e32 v[98:99], 0
	v_mov_b64_e32 v[96:97], 0
	v_mov_b64_e32 v[94:95], 0
	v_mov_b64_e32 v[88:89], 0
	v_mov_b64_e32 v[86:87], 0
	v_mov_b64_e32 v[80:81], 0
	v_mov_b64_e32 v[78:79], 0
	v_mov_b64_e32 v[72:73], 0
	v_mov_b64_e32 v[70:71], 0
	v_mov_b64_e32 v[64:65], 0
	v_mov_b64_e32 v[62:63], 0
	v_mov_b64_e32 v[56:57], 0
	v_mov_b64_e32 v[54:55], 0
	v_mov_b64_e32 v[48:49], 0
	v_mov_b64_e32 v[46:47], 0
	v_mov_b64_e32 v[40:41], 0
	v_mov_b64_e32 v[38:39], 0
	v_mov_b64_e32 v[92:93], 0
	v_mov_b64_e32 v[90:91], 0
	v_mov_b64_e32 v[84:85], 0
	v_mov_b64_e32 v[82:83], 0
	v_mov_b64_e32 v[76:77], 0
	v_mov_b64_e32 v[74:75], 0
	v_mov_b64_e32 v[68:69], 0
	v_mov_b64_e32 v[66:67], 0
	v_mov_b64_e32 v[60:61], 0
	v_mov_b64_e32 v[58:59], 0
	v_mov_b64_e32 v[52:53], 0
	v_mov_b64_e32 v[50:51], 0
	v_mov_b64_e32 v[44:45], 0
	v_mov_b64_e32 v[42:43], 0
	v_mov_b64_e32 v[36:37], 0
	v_mov_b64_e32 v[34:35], 0
	s_mov_b64 s[70:71], 0xe800800
	s_and_b64 vcc, exec, s[44:45]
	s_cbranch_vccnz .LBB0_1696
	s_branch .LBB0_1697

.LBB0_1776:
	v_lshl_add_u32 v250, s58, 8, v195
	v_lshlrev_b32_e32 v250, 2, v250
	global_load_dword v235, v250, s[36:37]
	global_load_dword v237, v250, s[36:37] offset:64
	global_load_dword v239, v250, s[36:37] offset:128
	global_load_dword v241, v250, s[36:37] offset:192
	global_load_dword v243, v250, s[36:37] offset:512
	global_load_dword v245, v250, s[36:37] offset:576
	global_load_dword v247, v250, s[36:37] offset:640
	global_load_dword v249, v250, s[36:37] offset:704
	global_load_dword v234, v250, s[40:41]
	global_load_dword v236, v250, s[40:41] offset:64
	global_load_dword v238, v250, s[40:41] offset:128
	global_load_dword v240, v250, s[40:41] offset:192
	global_load_dword v242, v250, s[40:41] offset:512
	global_load_dword v244, v250, s[40:41] offset:576
	global_load_dword v246, v250, s[40:41] offset:640
	global_load_dword v248, v250, s[40:41] offset:704
	s_add_u32 s51, s62, 0x100
	v_mov_b64_e32 v[70:71], 0
	v_mov_b32_e32 v1, 0x3ecc95a3
	s_addc_u32 s59, s63, 0
	s_mov_b32 s64, 0
	v_mov_b64_e32 v[72:73], 0
	v_mov_b64_e32 v[66:67], 0
	v_mov_b64_e32 v[68:69], 0
	v_mov_b64_e32 v[86:87], 0
	v_mov_b64_e32 v[88:89], 0
	v_mov_b64_e32 v[82:83], 0
	v_mov_b64_e32 v[84:85], 0
	v_mov_b64_e32 v[46:47], 0
	v_mov_b64_e32 v[48:49], 0
	v_mov_b64_e32 v[42:43], 0
	v_mov_b64_e32 v[44:45], 0
	v_mov_b64_e32 v[62:63], 0
	v_mov_b64_e32 v[64:65], 0
	v_mov_b64_e32 v[58:59], 0
	v_mov_b64_e32 v[60:61], 0
	v_mov_b64_e32 v[78:79], 0
	v_mov_b64_e32 v[80:81], 0
	v_mov_b64_e32 v[74:75], 0
	v_mov_b64_e32 v[76:77], 0
	v_mov_b64_e32 v[94:95], 0
	v_mov_b64_e32 v[96:97], 0
	v_mov_b64_e32 v[90:91], 0
	v_mov_b64_e32 v[92:93], 0
	v_mov_b64_e32 v[102:103], 0
	v_mov_b64_e32 v[104:105], 0
	v_mov_b64_e32 v[98:99], 0
	v_mov_b64_e32 v[100:101], 0
	v_mov_b64_e32 v[118:119], 0
	v_mov_b64_e32 v[120:121], 0
	v_mov_b64_e32 v[114:115], 0
	v_mov_b64_e32 v[116:117], 0
	v_mov_b64_e32 v[134:135], 0
	v_mov_b64_e32 v[136:137], 0
	v_mov_b64_e32 v[130:131], 0
	v_mov_b64_e32 v[132:133], 0
	v_mov_b64_e32 v[150:151], 0
	v_mov_b64_e32 v[152:153], 0
	v_mov_b64_e32 v[146:147], 0
	v_mov_b64_e32 v[148:149], 0
	v_mov_b64_e32 v[110:111], 0
	v_mov_b64_e32 v[112:113], 0
	v_mov_b64_e32 v[106:107], 0
	v_mov_b64_e32 v[108:109], 0
	v_mov_b64_e32 v[126:127], 0
	v_mov_b64_e32 v[128:129], 0
	v_mov_b64_e32 v[122:123], 0
	v_mov_b64_e32 v[124:125], 0
	v_mov_b64_e32 v[142:143], 0
	v_mov_b64_e32 v[144:145], 0
	v_mov_b64_e32 v[138:139], 0
	v_mov_b64_e32 v[140:141], 0
	v_mov_b64_e32 v[158:159], 0
	v_mov_b64_e32 v[160:161], 0
	v_mov_b64_e32 v[154:155], 0
	v_mov_b64_e32 v[156:157], 0
	v_mov_b64_e32 v[50:51], 0
	v_mov_b64_e32 v[52:53], 0
	v_mov_b64_e32 v[54:55], 0
	v_mov_b64_e32 v[56:57], 0
	v_mov_b64_e32 v[34:35], 0
	v_mov_b64_e32 v[36:37], 0
	v_mov_b64_e32 v[38:39], 0
	v_mov_b64_e32 v[40:41], 0

.LBB0_1801:
	v_lshl_add_u32 v250, s58, 8, v195
	v_lshlrev_b32_e32 v250, 2, v250
	global_load_dword v235, v250, s[36:37]
	global_load_dword v237, v250, s[36:37] offset:64
	global_load_dword v239, v250, s[36:37] offset:128
	global_load_dword v241, v250, s[36:37] offset:192
	global_load_dword v243, v250, s[36:37] offset:512
	global_load_dword v245, v250, s[36:37] offset:576
	global_load_dword v247, v250, s[36:37] offset:640
	global_load_dword v249, v250, s[36:37] offset:704
	global_load_dword v234, v250, s[40:41]
	global_load_dword v236, v250, s[40:41] offset:64
	global_load_dword v238, v250, s[40:41] offset:128
	global_load_dword v240, v250, s[40:41] offset:192
	global_load_dword v242, v250, s[40:41] offset:512
	global_load_dword v244, v250, s[40:41] offset:576
	global_load_dword v246, v250, s[40:41] offset:640
	global_load_dword v248, v250, s[40:41] offset:704
	s_waitcnt vmcnt(0)
	v_mov_b64_e32 v[40:41], 0
	v_mov_b64_e32 v[38:39], 0
	v_mov_b64_e32 v[36:37], 0
	v_mov_b64_e32 v[34:35], 0
	v_mov_b64_e32 v[56:57], 0
	v_mov_b64_e32 v[54:55], 0
	v_mov_b64_e32 v[52:53], 0
	v_mov_b64_e32 v[50:51], 0
	v_mov_b64_e32 v[156:157], 0
	v_mov_b64_e32 v[154:155], 0
	v_mov_b64_e32 v[160:161], 0
	v_mov_b64_e32 v[158:159], 0
	v_mov_b64_e32 v[140:141], 0
	v_mov_b64_e32 v[138:139], 0
	v_mov_b64_e32 v[144:145], 0
	v_mov_b64_e32 v[142:143], 0
	v_mov_b64_e32 v[124:125], 0
	v_mov_b64_e32 v[122:123], 0
	v_mov_b64_e32 v[128:129], 0
	v_mov_b64_e32 v[126:127], 0
	v_mov_b64_e32 v[108:109], 0
	v_mov_b64_e32 v[106:107], 0
	v_mov_b64_e32 v[112:113], 0
	v_mov_b64_e32 v[110:111], 0
	v_mov_b64_e32 v[148:149], 0
	v_mov_b64_e32 v[146:147], 0
	v_mov_b64_e32 v[152:153], 0
	v_mov_b64_e32 v[150:151], 0
	v_mov_b64_e32 v[132:133], 0
	v_mov_b64_e32 v[130:131], 0
	v_mov_b64_e32 v[136:137], 0
	v_mov_b64_e32 v[134:135], 0
	v_mov_b64_e32 v[116:117], 0
	v_mov_b64_e32 v[114:115], 0
	v_mov_b64_e32 v[120:121], 0
	v_mov_b64_e32 v[118:119], 0
	v_mov_b64_e32 v[100:101], 0
	v_mov_b64_e32 v[98:99], 0
	v_mov_b64_e32 v[104:105], 0
	v_mov_b64_e32 v[102:103], 0
	v_mov_b64_e32 v[92:93], 0
	v_mov_b64_e32 v[90:91], 0
	v_mov_b64_e32 v[96:97], 0
	v_mov_b64_e32 v[94:95], 0
	v_mov_b64_e32 v[76:77], 0
	v_mov_b64_e32 v[74:75], 0
	v_mov_b64_e32 v[80:81], 0
	v_mov_b64_e32 v[78:79], 0
	v_mov_b64_e32 v[60:61], 0
	v_mov_b64_e32 v[58:59], 0
	v_mov_b64_e32 v[64:65], 0
	v_mov_b64_e32 v[62:63], 0
	v_mov_b64_e32 v[44:45], 0
	v_mov_b64_e32 v[42:43], 0
	v_mov_b64_e32 v[48:49], 0
	v_mov_b64_e32 v[46:47], 0
	v_mov_b64_e32 v[84:85], 0
	v_mov_b64_e32 v[82:83], 0
	v_mov_b64_e32 v[88:89], 0
	v_mov_b64_e32 v[86:87], 0
	v_mov_b64_e32 v[68:69], 0
	v_mov_b64_e32 v[66:67], 0
	v_mov_b64_e32 v[72:73], 0
	v_mov_b64_e32 v[70:71], 0
	s_and_b64 vcc, exec, s[44:45]
	s_cbranch_vccnz .LBB0_1779
	s_branch .LBB0_1780

.LBB0_1834:
	s_andn2_b64 vcc, exec, s[40:41]
	s_cbranch_vccnz .LBB0_1840
	s_lshl_b32 s47, s48, 8
	v_add_u32_e32 v2, s47, v169
	v_add_u32_e32 v4, s47, v205
	s_bitset1_b32 s47, 7
	v_add_u32_e32 v6, s47, v169
	v_add_u32_e32 v8, s47, v205
	v_ashrrev_i32_e32 v3, 31, v2
	v_ashrrev_i32_e32 v5, 31, v4
	v_ashrrev_i32_e32 v7, 31, v6
	v_ashrrev_i32_e32 v9, 31, v8
	v_mov_b32_e32 v181, v167
	v_mov_b32_e32 v183, v167
	s_add_u32 s47, s60, 0x100
	v_mov_b64_e32 v[34:35], 0
	v_lshl_add_u64 v[184:185], v[2:3], 2, s[28:29]
	v_lshl_add_u64 v[186:187], v[4:5], 2, s[28:29]
	v_lshl_add_u64 v[188:189], v[6:7], 2, s[28:29]
	v_lshl_add_u64 v[190:191], v[8:9], 2, s[28:29]
	s_addc_u32 s49, s61, 0
	s_and_b64 vcc, exec, s[50:51]
	s_cbranch_vccz .Lnolist_17
	global_load_dword v184, v[184:185], off
	global_load_dword v186, v[186:187], off
	global_load_dword v188, v[188:189], off
	global_load_dword v190, v[190:191], off
.Lnolist_17:
	v_lshl_add_u64 v[192:193], s[38:39], 0, v[182:183]
	v_lshl_add_u64 v[194:195], s[38:39], 0, v[180:181]
	s_mov_b32 s55, 0
	s_mov_b64 s[64:65], 0
	v_mov_b64_e32 v[36:37], 0
	v_mov_b64_e32 v[42:43], 0
	v_mov_b64_e32 v[44:45], 0
	v_mov_b64_e32 v[50:51], 0
	v_mov_b64_e32 v[52:53], 0
	v_mov_b64_e32 v[58:59], 0
	v_mov_b64_e32 v[60:61], 0
	v_mov_b64_e32 v[66:67], 0
	v_mov_b64_e32 v[68:69], 0
	v_mov_b64_e32 v[74:75], 0
	v_mov_b64_e32 v[76:77], 0
	v_mov_b64_e32 v[82:83], 0
	v_mov_b64_e32 v[84:85], 0
	v_mov_b64_e32 v[90:91], 0
	v_mov_b64_e32 v[92:93], 0
	v_mov_b64_e32 v[38:39], 0
	v_mov_b64_e32 v[40:41], 0
	v_mov_b64_e32 v[46:47], 0
	v_mov_b64_e32 v[48:49], 0
	v_mov_b64_e32 v[54:55], 0
	v_mov_b64_e32 v[56:57], 0
	v_mov_b64_e32 v[62:63], 0
	v_mov_b64_e32 v[64:65], 0
	v_mov_b64_e32 v[70:71], 0
	v_mov_b64_e32 v[72:73], 0
	v_mov_b64_e32 v[78:79], 0
	v_mov_b64_e32 v[80:81], 0
	v_mov_b64_e32 v[86:87], 0
	v_mov_b64_e32 v[88:89], 0
	v_mov_b64_e32 v[94:95], 0
	v_mov_b64_e32 v[96:97], 0
	v_mov_b64_e32 v[98:99], 0
	v_mov_b64_e32 v[100:101], 0
	v_mov_b64_e32 v[106:107], 0
	v_mov_b64_e32 v[108:109], 0
	v_mov_b64_e32 v[114:115], 0
	v_mov_b64_e32 v[116:117], 0
	v_mov_b64_e32 v[122:123], 0
	v_mov_b64_e32 v[124:125], 0
	v_mov_b64_e32 v[130:131], 0
	v_mov_b64_e32 v[132:133], 0
	v_mov_b64_e32 v[138:139], 0
	v_mov_b64_e32 v[140:141], 0
	v_mov_b64_e32 v[146:147], 0
	v_mov_b64_e32 v[148:149], 0
	v_mov_b64_e32 v[158:159], 0
	v_mov_b64_e32 v[160:161], 0
	v_mov_b64_e32 v[102:103], 0
	v_mov_b64_e32 v[104:105], 0
	v_mov_b64_e32 v[110:111], 0
	v_mov_b64_e32 v[112:113], 0
	v_mov_b64_e32 v[118:119], 0
	v_mov_b64_e32 v[120:121], 0
	v_mov_b64_e32 v[126:127], 0
	v_mov_b64_e32 v[128:129], 0
	v_mov_b64_e32 v[134:135], 0
	v_mov_b64_e32 v[136:137], 0
	v_mov_b64_e32 v[142:143], 0
	v_mov_b64_e32 v[144:145], 0
	v_mov_b64_e32 v[150:151], 0
	v_mov_b64_e32 v[152:153], 0
	v_mov_b64_e32 v[154:155], 0
	v_mov_b64_e32 v[156:157], 0

.LBB0_1840:
	v_mov_b64_e32 v[156:157], 0
	v_mov_b64_e32 v[154:155], 0
	v_mov_b64_e32 v[152:153], 0
	v_mov_b64_e32 v[150:151], 0
	v_mov_b64_e32 v[144:145], 0
	v_mov_b64_e32 v[142:143], 0
	v_mov_b64_e32 v[136:137], 0
	v_mov_b64_e32 v[134:135], 0
	v_mov_b64_e32 v[128:129], 0
	v_mov_b64_e32 v[126:127], 0
	v_mov_b64_e32 v[120:121], 0
	v_mov_b64_e32 v[118:119], 0
	v_mov_b64_e32 v[112:113], 0
	v_mov_b64_e32 v[110:111], 0
	v_mov_b64_e32 v[104:105], 0
	v_mov_b64_e32 v[102:103], 0
	v_mov_b64_e32 v[160:161], 0
	v_mov_b64_e32 v[158:159], 0
	v_mov_b64_e32 v[148:149], 0
	v_mov_b64_e32 v[146:147], 0
	v_mov_b64_e32 v[140:141], 0
	v_mov_b64_e32 v[138:139], 0
	v_mov_b64_e32 v[132:133], 0
	v_mov_b64_e32 v[130:131], 0
	v_mov_b64_e32 v[124:125], 0
	v_mov_b64_e32 v[122:123], 0
	v_mov_b64_e32 v[116:117], 0
	v_mov_b64_e32 v[114:115], 0
	v_mov_b64_e32 v[108:109], 0
	v_mov_b64_e32 v[106:107], 0
	v_mov_b64_e32 v[100:101], 0
	v_mov_b64_e32 v[98:99], 0
	v_mov_b64_e32 v[96:97], 0
	v_mov_b64_e32 v[94:95], 0
	v_mov_b64_e32 v[88:89], 0
	v_mov_b64_e32 v[86:87], 0
	v_mov_b64_e32 v[80:81], 0
	v_mov_b64_e32 v[78:79], 0
	v_mov_b64_e32 v[72:73], 0
	v_mov_b64_e32 v[70:71], 0
	v_mov_b64_e32 v[64:65], 0
	v_mov_b64_e32 v[62:63], 0
	v_mov_b64_e32 v[56:57], 0
	v_mov_b64_e32 v[54:55], 0
	v_mov_b64_e32 v[48:49], 0
	v_mov_b64_e32 v[46:47], 0
	v_mov_b64_e32 v[40:41], 0
	v_mov_b64_e32 v[38:39], 0
	v_mov_b64_e32 v[92:93], 0
	v_mov_b64_e32 v[90:91], 0
	v_mov_b64_e32 v[84:85], 0
	v_mov_b64_e32 v[82:83], 0
	v_mov_b64_e32 v[76:77], 0
	v_mov_b64_e32 v[74:75], 0
	v_mov_b64_e32 v[68:69], 0
	v_mov_b64_e32 v[66:67], 0
	v_mov_b64_e32 v[60:61], 0
	v_mov_b64_e32 v[58:59], 0
	v_mov_b64_e32 v[52:53], 0
	v_mov_b64_e32 v[50:51], 0
	v_mov_b64_e32 v[44:45], 0
	v_mov_b64_e32 v[42:43], 0
	v_mov_b64_e32 v[36:37], 0
	v_mov_b64_e32 v[34:35], 0

.LBB0_1922:
	s_add_u32 s35, s70, 0x100
	v_mov_b64_e32 v[66:67], 0
	v_mov_b32_e32 v1, 0x3ecc95a3
	s_addc_u32 s45, s71, 0
	s_mov_b32 s70, 0
	v_mov_b64_e32 v[68:69], 0
	v_mov_b64_e32 v[70:71], 0
	v_mov_b64_e32 v[72:73], 0
	v_mov_b64_e32 v[82:83], 0
	v_mov_b64_e32 v[84:85], 0
	v_mov_b64_e32 v[86:87], 0
	v_mov_b64_e32 v[88:89], 0
	v_mov_b64_e32 v[42:43], 0
	v_mov_b64_e32 v[44:45], 0
	v_mov_b64_e32 v[46:47], 0
	v_mov_b64_e32 v[48:49], 0
	v_mov_b64_e32 v[58:59], 0
	v_mov_b64_e32 v[60:61], 0
	v_mov_b64_e32 v[62:63], 0
	v_mov_b64_e32 v[64:65], 0
	v_mov_b64_e32 v[74:75], 0
	v_mov_b64_e32 v[76:77], 0
	v_mov_b64_e32 v[78:79], 0
	v_mov_b64_e32 v[80:81], 0
	v_mov_b64_e32 v[90:91], 0
	v_mov_b64_e32 v[92:93], 0
	v_mov_b64_e32 v[94:95], 0
	v_mov_b64_e32 v[96:97], 0
	v_mov_b64_e32 v[98:99], 0
	v_mov_b64_e32 v[100:101], 0
	v_mov_b64_e32 v[102:103], 0
	v_mov_b64_e32 v[104:105], 0
	v_mov_b64_e32 v[114:115], 0
	v_mov_b64_e32 v[116:117], 0
	v_mov_b64_e32 v[118:119], 0
	v_mov_b64_e32 v[120:121], 0
	v_mov_b64_e32 v[130:131], 0
	v_mov_b64_e32 v[132:133], 0
	v_mov_b64_e32 v[134:135], 0
	v_mov_b64_e32 v[136:137], 0
	v_mov_b64_e32 v[146:147], 0
	v_mov_b64_e32 v[148:149], 0
	v_mov_b64_e32 v[150:151], 0
	v_mov_b64_e32 v[152:153], 0
	v_mov_b64_e32 v[106:107], 0
	v_mov_b64_e32 v[108:109], 0
	v_mov_b64_e32 v[110:111], 0
	v_mov_b64_e32 v[112:113], 0
	v_mov_b64_e32 v[122:123], 0
	v_mov_b64_e32 v[124:125], 0
	v_mov_b64_e32 v[126:127], 0
	v_mov_b64_e32 v[128:129], 0
	v_mov_b64_e32 v[138:139], 0
	v_mov_b64_e32 v[140:141], 0
	v_mov_b64_e32 v[142:143], 0
	v_mov_b64_e32 v[144:145], 0
	v_mov_b64_e32 v[154:155], 0
	v_mov_b64_e32 v[156:157], 0
	v_mov_b64_e32 v[158:159], 0
	v_mov_b64_e32 v[160:161], 0
	v_mov_b64_e32 v[54:55], 0
	v_mov_b64_e32 v[56:57], 0
	v_mov_b64_e32 v[50:51], 0
	v_mov_b64_e32 v[52:53], 0
	v_mov_b64_e32 v[38:39], 0
	v_mov_b64_e32 v[40:41], 0
	v_mov_b64_e32 v[34:35], 0
	v_mov_b64_e32 v[36:37], 0

.LBB0_1934:
	v_mov_b64_e32 v[36:37], 0
	v_mov_b64_e32 v[34:35], 0
	v_mov_b64_e32 v[40:41], 0
	v_mov_b64_e32 v[38:39], 0
	v_mov_b64_e32 v[52:53], 0
	v_mov_b64_e32 v[50:51], 0
	v_mov_b64_e32 v[56:57], 0
	v_mov_b64_e32 v[54:55], 0
	v_mov_b64_e32 v[160:161], 0
	v_mov_b64_e32 v[158:159], 0
	v_mov_b64_e32 v[156:157], 0
	v_mov_b64_e32 v[154:155], 0
	v_mov_b64_e32 v[144:145], 0
	v_mov_b64_e32 v[142:143], 0
	v_mov_b64_e32 v[140:141], 0
	v_mov_b64_e32 v[138:139], 0
	v_mov_b64_e32 v[128:129], 0
	v_mov_b64_e32 v[126:127], 0
	v_mov_b64_e32 v[124:125], 0
	v_mov_b64_e32 v[122:123], 0
	v_mov_b64_e32 v[112:113], 0
	v_mov_b64_e32 v[110:111], 0
	v_mov_b64_e32 v[108:109], 0
	v_mov_b64_e32 v[106:107], 0
	v_mov_b64_e32 v[152:153], 0
	v_mov_b64_e32 v[150:151], 0
	v_mov_b64_e32 v[148:149], 0
	v_mov_b64_e32 v[146:147], 0
	v_mov_b64_e32 v[136:137], 0
	v_mov_b64_e32 v[134:135], 0
	v_mov_b64_e32 v[132:133], 0
	v_mov_b64_e32 v[130:131], 0
	v_mov_b64_e32 v[120:121], 0
	v_mov_b64_e32 v[118:119], 0
	v_mov_b64_e32 v[116:117], 0
	v_mov_b64_e32 v[114:115], 0
	v_mov_b64_e32 v[104:105], 0
	v_mov_b64_e32 v[102:103], 0
	v_mov_b64_e32 v[100:101], 0
	v_mov_b64_e32 v[98:99], 0
	v_mov_b64_e32 v[96:97], 0
	v_mov_b64_e32 v[94:95], 0
	v_mov_b64_e32 v[92:93], 0
	v_mov_b64_e32 v[90:91], 0
	v_mov_b64_e32 v[80:81], 0
	v_mov_b64_e32 v[78:79], 0
	v_mov_b64_e32 v[76:77], 0
	v_mov_b64_e32 v[74:75], 0
	v_mov_b64_e32 v[64:65], 0
	v_mov_b64_e32 v[62:63], 0
	v_mov_b64_e32 v[60:61], 0
	v_mov_b64_e32 v[58:59], 0
	v_mov_b64_e32 v[48:49], 0
	v_mov_b64_e32 v[46:47], 0
	v_mov_b64_e32 v[44:45], 0
	v_mov_b64_e32 v[42:43], 0
	v_mov_b64_e32 v[88:89], 0
	v_mov_b64_e32 v[86:87], 0
	v_mov_b64_e32 v[84:85], 0
	v_mov_b64_e32 v[82:83], 0
	v_mov_b64_e32 v[72:73], 0
	v_mov_b64_e32 v[70:71], 0
	v_mov_b64_e32 v[68:69], 0
	v_mov_b64_e32 v[66:67], 0
	s_andn2_b64 vcc, exec, s[58:59]
	s_cbranch_vccz .LBB0_1925
	s_branch .LBB0_1926
